# attention key loop: one static s_setprio 1 for waves 4-7 before the loop, reset at the unit epilogue (on top of v102)
# baseline (speedup 1.0000x reference)
.LBB0_950:
	s_setprio 0
	s_waitcnt vmcnt(0)
	v_readfirstlane_b32 s38, v241
	v_mov_b32_e32 v48, v173
	s_nop 1
	v_permlane32_swap_b32_e32 v173, v48
	v_add_f32_e32 v48, v173, v48
	v_div_scale_f32 v49, s[14:15], v48, v48, 1.0
	v_rcp_f32_e32 v50, v49
	s_lshl_b32 s64, s23, 7
	v_lshlrev_b32_e32 v208, 2, v188
	s_mov_b64 s[14:15], 0x23c00200
	v_fma_f32 v51, -v49, v50, 1.0
	v_fmac_f32_e32 v50, v51, v50
	v_div_scale_f32 v51, vcc, 1.0, v48, 1.0
	v_mul_f32_e32 v52, v51, v50
	v_fma_f32 v53, -v49, v52, v51
	v_fmac_f32_e32 v52, v53, v50
	v_fma_f32 v49, -v49, v52, v51
	v_div_fmas_f32 v49, v49, v50, v52
	v_lshlrev_b64 v[50:51], 11, v[200:201]
	v_lshl_add_u64 v[50:51], s[8:9], 0, v[50:51]
	v_lshl_add_u64 v[50:51], v[50:51], 0, s[64:65]
	v_div_fixup_f32 v48, v49, v48, 1.0
	v_lshl_add_u64 v[50:51], v[50:51], 0, v[208:209]
	v_lshl_add_u64 v[52:53], v[50:51], 0, s[14:15]
	v_pk_mul_f32 v[32:33], v[32:33], v[48:49] op_sel_hi:[1,0]
	v_pk_mul_f32 v[34:35], v[34:35], v[48:49] op_sel_hi:[1,0]
	v_pk_mul_f32 v[36:37], v[36:37], v[48:49] op_sel_hi:[1,0]
	v_pk_mul_f32 v[38:39], v[38:39], v[48:49] op_sel_hi:[1,0]
	v_cvt_pk_bf16_f32 v32, v32, v33
	v_cvt_pk_bf16_f32 v33, v34, v35
	v_cvt_pk_bf16_f32 v34, v36, v37
	v_cvt_pk_bf16_f32 v35, v38, v39
	v_pk_mul_f32 v[16:17], v[16:17], v[48:49] op_sel_hi:[1,0]
	v_pk_mul_f32 v[18:19], v[18:19], v[48:49] op_sel_hi:[1,0]
	v_pk_mul_f32 v[20:21], v[20:21], v[48:49] op_sel_hi:[1,0]
	v_pk_mul_f32 v[22:23], v[22:23], v[48:49] op_sel_hi:[1,0]
	v_cvt_pk_bf16_f32 v16, v16, v17
	v_cvt_pk_bf16_f32 v17, v18, v19
	v_cvt_pk_bf16_f32 v18, v20, v21
	v_cvt_pk_bf16_f32 v19, v22, v23
	v_permlane32_swap_b32_e32 v32, v34
	v_permlane32_swap_b32_e32 v33, v35
	global_store_dwordx4 v[52:53], v[32:35], off
	v_pk_mul_f32 v[40:41], v[40:41], v[48:49] op_sel_hi:[1,0]
	v_pk_mul_f32 v[42:43], v[42:43], v[48:49] op_sel_hi:[1,0]
	v_pk_mul_f32 v[44:45], v[44:45], v[48:49] op_sel_hi:[1,0]
	v_pk_mul_f32 v[46:47], v[46:47], v[48:49] op_sel_hi:[1,0]
	v_cvt_pk_bf16_f32 v40, v40, v41
	v_cvt_pk_bf16_f32 v41, v42, v43
	v_cvt_pk_bf16_f32 v42, v44, v45
	v_cvt_pk_bf16_f32 v43, v46, v47
	v_permlane32_swap_b32_e32 v16, v18
	v_permlane32_swap_b32_e32 v17, v19
	global_store_dwordx4 v[52:53], v[16:19], off offset:64
	v_pk_mul_f32 v[24:25], v[24:25], v[48:49] op_sel_hi:[1,0]
	v_pk_mul_f32 v[26:27], v[26:27], v[48:49] op_sel_hi:[1,0]
	v_pk_mul_f32 v[28:29], v[28:29], v[48:49] op_sel_hi:[1,0]
	v_pk_mul_f32 v[30:31], v[30:31], v[48:49] op_sel_hi:[1,0]
	v_cvt_pk_bf16_f32 v24, v24, v25
	v_cvt_pk_bf16_f32 v25, v26, v27
	v_cvt_pk_bf16_f32 v26, v28, v29
	v_cvt_pk_bf16_f32 v27, v30, v31
	v_permlane32_swap_b32_e32 v40, v42
	v_permlane32_swap_b32_e32 v41, v43
	global_store_dwordx4 v[52:53], v[40:43], off offset:32
	s_mov_b64 s[14:15], 0
	s_nop 1
	v_permlane32_swap_b32_e32 v24, v26
	v_permlane32_swap_b32_e32 v25, v27
	global_store_dwordx4 v[52:53], v[24:27], off offset:96

.LBB0_967:
	s_or_b64 exec, exec, s[18:19]
	v_add_f32_e32 v80, v154, v155
	v_fmamk_f32 v80, v80, 0x3c2aaaab, v210
	v_mul_f32_e32 v81, 0x4b800000, v80
	v_cmp_gt_f32_e32 vcc, s56, v80
	s_mov_b32 s18, 0x3e16c740
	s_lshl_b32 s25, s25, 2
	v_cndmask_b32_e32 v80, v80, v81, vcc
	v_rsq_f32_e32 v80, v80
	s_add_i32 s26, s25, 4
	s_mov_b32 s30, 0
	v_lshl_add_u64 v[202:203], v[166:167], 1, s[16:17]
	v_mul_f32_e32 v81, 0x45800000, v80
	v_cndmask_b32_e32 v80, v80, v81, vcc
	v_mul_f32_e32 v82, 0x3e16c740, v80
	s_waitcnt vmcnt(10)
	v_pk_mul_f32 v[52:53], v[52:53], v[82:83] op_sel_hi:[1,0]
	v_pk_mul_f32 v[88:89], v[88:89], v[82:83] op_sel_hi:[1,0]
	v_pk_mul_f32 v[52:53], v[52:53], v[124:125]
	v_pk_mul_f32 v[90:91], v[90:91], v[82:83] op_sel_hi:[1,0]
	v_cvt_pk_bf16_f32 v102, v52, v53
	v_pk_mul_f32 v[52:53], v[80:81], v[106:107] op_sel_hi:[0,1]
	global_load_dwordx4 v[104:107], v[198:199], off offset:256
	s_waitcnt vmcnt(8)
	v_pk_mul_f32 v[36:37], v[36:37], v[52:53]
	v_pk_mul_f32 v[52:53], v[80:81], v[120:121] op_sel_hi:[0,1]
	s_waitcnt vmcnt(6)
	v_pk_mul_f32 v[32:33], v[52:53], v[32:33]
	v_pk_mul_f32 v[76:77], v[76:77], v[82:83] op_sel_hi:[1,0]
	s_waitcnt vmcnt(2)
	v_pk_mul_f32 v[52:53], v[44:45], v[32:33]
	v_pk_mul_f32 v[32:33], v[40:41], v[32:33]
	v_pk_fma_f32 v[52:53], v[40:41], v[36:37], v[52:53] neg_lo:[0,0,1] neg_hi:[0,0,1]
	v_pk_fma_f32 v[32:33], v[44:45], v[36:37], v[32:33]
	v_pk_mul_f32 v[36:37], v[80:81], v[116:117] op_sel_hi:[0,1]
	v_pk_mul_f32 v[36:37], v[38:39], v[36:37]
	v_pk_mul_f32 v[38:39], v[80:81], v[118:119] op_sel_hi:[0,1]
	v_pk_mul_f32 v[34:35], v[38:39], v[34:35]
	v_pk_mul_f32 v[32:33], v[32:33], s[18:19] op_sel_hi:[1,0]
	v_pk_mul_f32 v[38:39], v[46:47], v[34:35]
	v_pk_mul_f32 v[34:35], v[42:43], v[34:35]
	v_pk_fma_f32 v[38:39], v[42:43], v[36:37], v[38:39] neg_lo:[0,0,1] neg_hi:[0,0,1]
	v_pk_fma_f32 v[34:35], v[46:47], v[36:37], v[34:35]
	v_pk_mul_f32 v[36:37], v[80:81], v[112:113] op_sel_hi:[0,1]
	v_pk_mul_f32 v[16:17], v[36:37], v[16:17]
	v_pk_mul_f32 v[36:37], v[80:81], v[114:115] op_sel_hi:[0,1]
	v_pk_mul_f32 v[20:21], v[36:37], v[20:21]
	v_cvt_pk_bf16_f32 v112, v32, v33
	v_pk_mul_f32 v[36:37], v[28:29], v[20:21]
	v_pk_mul_f32 v[20:21], v[24:25], v[20:21]
	v_pk_fma_f32 v[36:37], v[24:25], v[16:17], v[36:37] neg_lo:[0,0,1] neg_hi:[0,0,1]
	v_pk_fma_f32 v[16:17], v[28:29], v[16:17], v[20:21]
	v_pk_mul_f32 v[20:21], v[80:81], v[108:109] op_sel_hi:[0,1]
	v_pk_mul_f32 v[18:19], v[20:21], v[18:19]
	v_pk_mul_f32 v[20:21], v[80:81], v[110:111] op_sel_hi:[0,1]
	v_pk_mul_f32 v[20:21], v[20:21], v[22:23]
	v_mov_b32_e32 v32, v209
	v_pk_mul_f32 v[22:23], v[30:31], v[20:21]
	v_pk_mul_f32 v[20:21], v[26:27], v[20:21]
	v_pk_fma_f32 v[22:23], v[26:27], v[18:19], v[22:23] neg_lo:[0,0,1] neg_hi:[0,0,1]
	v_pk_fma_f32 v[18:19], v[30:31], v[18:19], v[20:21]
	v_pk_mul_f32 v[78:79], v[78:79], v[82:83] op_sel_hi:[1,0]
	v_pk_mul_f32 v[72:73], v[72:73], v[82:83] op_sel_hi:[1,0]
	v_pk_mul_f32 v[74:75], v[74:75], v[82:83] op_sel_hi:[1,0]
	v_pk_mul_f32 v[68:69], v[68:69], v[82:83] op_sel_hi:[1,0]
	v_pk_mul_f32 v[70:71], v[70:71], v[82:83] op_sel_hi:[1,0]
	v_pk_mul_f32 v[64:65], v[64:65], v[82:83] op_sel_hi:[1,0]
	v_pk_mul_f32 v[66:67], v[66:67], v[82:83] op_sel_hi:[1,0]
	v_pk_mul_f32 v[60:61], v[60:61], v[82:83] op_sel_hi:[1,0]
	v_pk_mul_f32 v[62:63], v[62:63], v[82:83] op_sel_hi:[1,0]
	v_pk_mul_f32 v[56:57], v[56:57], v[82:83] op_sel_hi:[1,0]
	v_pk_mul_f32 v[58:59], v[58:59], v[82:83] op_sel_hi:[1,0]
	v_pk_mul_f32 v[54:55], v[54:55], v[82:83] op_sel_hi:[1,0]
	v_pk_mul_f32 v[38:39], v[38:39], s[18:19] op_sel_hi:[1,0]
	v_pk_mul_f32 v[34:35], v[34:35], s[18:19] op_sel_hi:[1,0]
	v_pk_mul_f32 v[36:37], v[36:37], s[18:19] op_sel_hi:[1,0]
	v_pk_mul_f32 v[16:17], v[16:17], s[18:19] op_sel_hi:[1,0]
	v_pk_mul_f32 v[22:23], v[22:23], s[18:19] op_sel_hi:[1,0]
	v_pk_mul_f32 v[18:19], v[18:19], s[18:19] op_sel_hi:[1,0]
	s_waitcnt lgkmcnt(0)
	s_barrier
	v_pk_mul_f32 v[88:89], v[88:89], v[152:153]
	v_mov_b32_e32 v33, v32
	v_pk_mul_f32 v[90:91], v[90:91], v[150:151]
	v_pk_mul_f32 v[76:77], v[76:77], v[148:149]
	v_pk_mul_f32 v[78:79], v[78:79], v[146:147]
	v_pk_mul_f32 v[72:73], v[72:73], v[144:145]
	v_pk_mul_f32 v[74:75], v[74:75], v[142:143]
	v_pk_mul_f32 v[68:69], v[68:69], v[140:141]
	v_pk_mul_f32 v[70:71], v[70:71], v[138:139]
	v_pk_mul_f32 v[64:65], v[64:65], v[136:137]
	v_pk_mul_f32 v[66:67], v[66:67], v[134:135]
	v_pk_mul_f32 v[60:61], v[60:61], v[132:133]
	v_pk_mul_f32 v[62:63], v[62:63], v[130:131]
	v_pk_mul_f32 v[56:57], v[56:57], v[128:129]
	v_pk_mul_f32 v[58:59], v[58:59], v[126:127]
	v_pk_mul_f32 v[54:55], v[54:55], v[122:123]
	v_pk_mul_f32 v[52:53], v[52:53], s[18:19] op_sel_hi:[1,0]
	v_cvt_pk_bf16_f32 v109, v38, v39
	v_cvt_pk_bf16_f32 v110, v36, v37
	v_cvt_pk_bf16_f32 v111, v22, v23
	v_cvt_pk_bf16_f32 v113, v34, v35
	v_cvt_pk_bf16_f32 v114, v16, v17
	v_cvt_pk_bf16_f32 v115, v18, v19
	v_mov_b32_e32 v34, v32
	v_mov_b32_e32 v35, v32
	v_mov_b32_e32 v36, v32
	v_mov_b32_e32 v37, v32
	v_mov_b32_e32 v38, v32
	v_mov_b32_e32 v39, v32
	v_mov_b32_e32 v40, v32
	v_mov_b32_e32 v41, v32
	v_mov_b32_e32 v42, v32
	v_mov_b32_e32 v43, v32
	v_mov_b32_e32 v44, v32
	v_mov_b32_e32 v45, v32
	v_mov_b32_e32 v46, v32
	v_mov_b32_e32 v47, v32
	v_mov_b64_e32 v[16:17], v[32:33]
	s_waitcnt vmcnt(1)
	v_mov_b64_e32 v[82:83], v[50:51]
	v_cvt_pk_bf16_f32 v88, v88, v89
	v_cvt_pk_bf16_f32 v89, v90, v91
	v_cvt_pk_bf16_f32 v90, v76, v77
	v_cvt_pk_bf16_f32 v91, v78, v79
	v_cvt_pk_bf16_f32 v92, v72, v73
	v_cvt_pk_bf16_f32 v93, v74, v75
	v_cvt_pk_bf16_f32 v94, v68, v69
	v_cvt_pk_bf16_f32 v95, v70, v71
	v_cvt_pk_bf16_f32 v96, v64, v65
	v_cvt_pk_bf16_f32 v97, v66, v67
	v_cvt_pk_bf16_f32 v98, v60, v61
	v_cvt_pk_bf16_f32 v99, v62, v63
	v_cvt_pk_bf16_f32 v100, v56, v57
	v_cvt_pk_bf16_f32 v101, v58, v59
	v_cvt_pk_bf16_f32 v103, v54, v55
	v_cvt_pk_bf16_f32 v108, v52, v53
	s_or_b32 s27, s24, 31
	v_lshl_add_u64 v[204:205], v[170:171], 1, s[16:17]
	v_or_b32_e32 v223, s24, v160
	v_lshl_add_u64 v[206:207], v[192:193], 0, s[64:65]
	v_lshl_add_u64 v[216:217], v[194:195], 0, s[14:15]
	v_lshl_add_u64 v[218:219], v[196:197], 0, s[14:15]
	v_mov_b32_e32 v173, 0
	s_movk_i32 s28, 0x7f
	v_mov_b64_e32 v[18:19], v[34:35]
	v_mov_b64_e32 v[20:21], v[36:37]
	v_mov_b64_e32 v[22:23], v[38:39]
	v_mov_b64_e32 v[24:25], v[40:41]
	v_mov_b64_e32 v[26:27], v[42:43]
	v_mov_b64_e32 v[28:29], v[44:45]
	v_mov_b64_e32 v[30:31], v[46:47]
	v_mov_b64_e32 v[80:81], v[48:49]
	s_cmp_lg_u64 s[2:3], 0
	s_cbranch_scc1 .Lprio_done
	s_setprio 1
.Lprio_done:
	s_mov_b64 s[34:35], 0x3000
